# in-projection epilogue: nt on the fp8 merge-gate stores only (consumed three phases later)
# baseline (speedup 1.0000x reference)
.LBB0_281:
	v_pk_mul_f32 v[142:143], v[122:123], s[44:45] op_sel_hi:[1,0]
	v_mov_b32_e32 v123, v131
	v_cvt_pk_fp8_f32 v123, v142, v143
	v_pk_mul_f32 v[124:125], v[124:125], s[44:45] op_sel_hi:[1,0]
	v_pk_mul_f32 v[114:115], v[114:115], s[44:45] op_sel_hi:[1,0]
	v_pk_mul_f32 v[116:117], v[116:117], s[44:45] op_sel_hi:[1,0]
	v_cvt_pk_fp8_f32 v123, v124, v125 op_sel:[0,0,1]
	v_mov_b32_e32 v125, v131
	v_cvt_pk_fp8_f32 v125, v114, v115
	v_pk_mul_f32 v[108:109], v[108:109], s[44:45] op_sel_hi:[1,0]
	v_pk_mul_f32 v[98:99], v[98:99], s[44:45] op_sel_hi:[1,0]
	v_pk_mul_f32 v[90:91], v[90:91], s[44:45] op_sel_hi:[1,0]
	v_cvt_pk_fp8_f32 v125, v116, v117 op_sel:[0,0,1]
	v_pk_mul_f32 v[116:117], v[106:107], s[44:45] op_sel_hi:[1,0]
	v_mov_b32_e32 v107, v131
	v_cvt_pk_fp8_f32 v107, v116, v117
	v_pk_mul_f32 v[92:93], v[92:93], s[44:45] op_sel_hi:[1,0]
	v_pk_mul_f32 v[82:83], v[82:83], s[44:45] op_sel_hi:[1,0]
	v_pk_mul_f32 v[74:75], v[74:75], s[44:45] op_sel_hi:[1,0]
	v_cvt_pk_fp8_f32 v107, v108, v109 op_sel:[0,0,1]
	v_mov_b32_e32 v108, v131
	v_mov_b32_e32 v109, v131
	v_cvt_pk_fp8_f32 v108, v98, v99
	v_cvt_pk_fp8_f32 v109, v90, v91
	v_pk_mul_f32 v[90:91], v[100:101], s[44:45] op_sel_hi:[1,0]
	v_pk_mul_f32 v[76:77], v[76:77], s[44:45] op_sel_hi:[1,0]
	v_cvt_pk_fp8_f32 v108, v90, v91 op_sel:[0,0,1]
	v_cvt_pk_fp8_f32 v109, v92, v93 op_sel:[0,0,1]
	v_pk_mul_f32 v[92:93], v[102:103], s[44:45] op_sel_hi:[1,0]
	v_mov_b32_e32 v90, v131
	v_cvt_pk_fp8_f32 v90, v92, v93
	v_pk_mul_f32 v[92:93], v[104:105], s[44:45] op_sel_hi:[1,0]
	v_pk_mul_f32 v[62:63], v[62:63], s[44:45] op_sel_hi:[1,0]
	v_pk_mul_f32 v[58:59], v[58:59], s[44:45] op_sel_hi:[1,0]
	v_cvt_pk_fp8_f32 v90, v92, v93 op_sel:[0,0,1]
	v_mov_b32_e32 v92, v131
	v_mov_b32_e32 v93, v131
	v_cvt_pk_fp8_f32 v92, v82, v83
	v_cvt_pk_fp8_f32 v93, v74, v75
	v_pk_mul_f32 v[74:75], v[84:85], s[44:45] op_sel_hi:[1,0]
	v_pk_mul_f32 v[46:47], v[46:47], s[44:45] op_sel_hi:[1,0]
	v_cvt_pk_fp8_f32 v92, v74, v75 op_sel:[0,0,1]
	v_cvt_pk_fp8_f32 v93, v76, v77 op_sel:[0,0,1]
	v_pk_mul_f32 v[76:77], v[86:87], s[44:45] op_sel_hi:[1,0]
	v_mov_b32_e32 v74, v131
	v_cvt_pk_fp8_f32 v74, v76, v77
	v_pk_mul_f32 v[76:77], v[88:89], s[44:45] op_sel_hi:[1,0]
	v_pk_mul_f32 v[44:45], v[44:45], s[44:45] op_sel_hi:[1,0]
	v_pk_mul_f32 v[30:31], v[30:31], s[44:45] op_sel_hi:[1,0]
	v_cvt_pk_fp8_f32 v74, v76, v77 op_sel:[0,0,1]
	v_mov_b32_e32 v76, v131
	v_cvt_pk_fp8_f32 v76, v62, v63
	v_mov_b32_e32 v77, v131
	v_cvt_pk_fp8_f32 v77, v58, v59
	v_pk_mul_f32 v[58:59], v[64:65], s[44:45] op_sel_hi:[1,0]
	v_pk_mul_f32 v[20:21], v[20:21], s[44:45] op_sel_hi:[1,0]
	v_cvt_pk_fp8_f32 v76, v58, v59 op_sel:[0,0,1]
	v_pk_mul_f32 v[58:59], v[42:43], s[44:45] op_sel_hi:[1,0]
	v_mov_b32_e32 v43, v131
	v_cvt_pk_fp8_f32 v43, v58, v59
	v_mov_b32_e32 v42, v131
	v_cvt_pk_fp8_f32 v42, v46, v47
	v_pk_mul_f32 v[46:47], v[48:49], s[44:45] op_sel_hi:[1,0]
	v_cvt_pk_fp8_f32 v43, v44, v45 op_sel:[0,0,1]
	v_pk_mul_f32 v[48:49], v[70:71], s[44:45] op_sel_hi:[1,0]
	v_mov_b32_e32 v45, v131
	v_cvt_pk_fp8_f32 v45, v48, v49
	v_pk_mul_f32 v[48:49], v[72:73], s[44:45] op_sel_hi:[1,0]
	v_pk_mul_f32 v[14:15], v[14:15], s[44:45] op_sel_hi:[1,0]
	v_pk_mul_f32 v[12:13], v[12:13], s[44:45] op_sel_hi:[1,0]
	v_cvt_pk_fp8_f32 v45, v48, v49 op_sel:[0,0,1]
	v_pk_mul_f32 v[48:49], v[18:19], s[44:45] op_sel_hi:[1,0]
	v_mov_b32_e32 v18, v131
	v_mov_b32_e32 v19, v131
	v_cvt_pk_fp8_f32 v18, v30, v31
	v_cvt_pk_fp8_f32 v19, v48, v49
	v_pk_mul_f32 v[30:31], v[32:33], s[44:45] op_sel_hi:[1,0]
	v_pk_mul_f32 v[6:7], v[6:7], s[44:45] op_sel_hi:[1,0]
	v_cvt_pk_fp8_f32 v18, v30, v31 op_sel:[0,0,1]
	v_cvt_pk_fp8_f32 v19, v20, v21 op_sel:[0,0,1]
	v_pk_mul_f32 v[30:31], v[50:51], s[44:45] op_sel_hi:[1,0]
	v_mov_b32_e32 v20, v131
	v_cvt_pk_fp8_f32 v20, v30, v31
	v_pk_mul_f32 v[30:31], v[52:53], s[44:45] op_sel_hi:[1,0]
	s_lshl_b32 s6, s92, 3
	s_add_i32 s6, s93, s6
	v_cvt_pk_fp8_f32 v20, v30, v31 op_sel:[0,0,1]
	v_pk_mul_f32 v[30:31], v[10:11], s[44:45] op_sel_hi:[1,0]
	v_mov_b32_e32 v10, v131
	v_mov_b32_e32 v11, v131
	v_cvt_pk_fp8_f32 v10, v14, v15
	v_cvt_pk_fp8_f32 v11, v30, v31
	v_pk_mul_f32 v[14:15], v[16:17], s[44:45] op_sel_hi:[1,0]
	v_pk_mul_f32 v[126:127], v[126:127], s[44:45] op_sel_hi:[1,0]
	v_cvt_pk_fp8_f32 v10, v14, v15 op_sel:[0,0,1]
	v_cvt_pk_fp8_f32 v11, v12, v13 op_sel:[0,0,1]
	v_pk_mul_f32 v[14:15], v[34:35], s[44:45] op_sel_hi:[1,0]
	v_mov_b32_e32 v12, v131
	v_cvt_pk_fp8_f32 v12, v14, v15
	v_pk_mul_f32 v[14:15], v[36:37], s[44:45] op_sel_hi:[1,0]
	v_mov_b32_e32 v122, v131
	v_pk_mul_f32 v[118:119], v[118:119], s[44:45] op_sel_hi:[1,0]
	v_cvt_pk_fp8_f32 v12, v14, v15 op_sel:[0,0,1]
	v_pk_mul_f32 v[14:15], v[2:3], s[44:45] op_sel_hi:[1,0]
	v_mov_b32_e32 v2, v131
	v_mov_b32_e32 v3, v131
	v_cvt_pk_fp8_f32 v2, v6, v7
	v_cvt_pk_fp8_f32 v3, v14, v15
	v_mov_b32_e32 v124, v131
	v_cvt_pk_fp8_f32 v42, v46, v47 op_sel:[0,0,1]
	v_pk_mul_f32 v[46:47], v[66:67], s[44:45] op_sel_hi:[1,0]
	v_mov_b32_e32 v44, v131
	s_add_i32 s34, s6, -10
	v_cvt_pk_fp8_f32 v122, v126, v127
	v_cvt_pk_fp8_f32 v124, v118, v119
	v_pk_mul_f32 v[110:111], v[110:111], s[44:45] op_sel_hi:[1,0]
	v_mov_b32_e32 v106, v131
	v_cvt_pk_fp8_f32 v44, v46, v47
	v_pk_mul_f32 v[32:33], v[54:55], s[44:45] op_sel_hi:[1,0]
	v_mov_b32_e32 v21, v131
	s_ashr_i32 s35, s34, 31
	v_cvt_pk_fp8_f32 v106, v110, v111
	v_pk_mul_f32 v[94:95], v[94:95], s[44:45] op_sel_hi:[1,0]
	v_mov_b32_e32 v91, v131
	v_cvt_pk_fp8_f32 v21, v32, v33
	v_pk_mul_f32 v[16:17], v[38:39], s[44:45] op_sel_hi:[1,0]
	v_mov_b32_e32 v13, v131
	v_pk_mul_f32 v[6:7], v[8:9], s[44:45] op_sel_hi:[1,0]
	v_pk_mul_f32 v[4:5], v[4:5], s[44:45] op_sel_hi:[1,0]
	s_lshl_b64 s[34:35], s[34:35], 16
	v_cvt_pk_fp8_f32 v91, v94, v95
	v_pk_mul_f32 v[78:79], v[78:79], s[44:45] op_sel_hi:[1,0]
	v_mov_b32_e32 v75, v131
	v_cvt_pk_fp8_f32 v13, v16, v17
	v_cvt_pk_fp8_f32 v2, v6, v7 op_sel:[0,0,1]
	v_cvt_pk_fp8_f32 v3, v4, v5 op_sel:[0,0,1]
	v_pk_mul_f32 v[6:7], v[22:23], s[44:45] op_sel_hi:[1,0]
	v_pk_mul_f32 v[8:9], v[26:27], s[44:45] op_sel_hi:[1,0]
	v_mov_b32_e32 v4, v131
	v_mov_b32_e32 v5, v131
	v_pk_mul_f32 v[126:127], v[128:129], s[44:45] op_sel_hi:[1,0]
	v_pk_mul_f32 v[114:115], v[120:121], s[44:45] op_sel_hi:[1,0]
	s_add_u32 s34, s87, s34
	v_cvt_pk_fp8_f32 v75, v78, v79
	v_pk_mul_f32 v[46:47], v[68:69], s[44:45] op_sel_hi:[1,0]
	v_cvt_pk_fp8_f32 v4, v6, v7
	v_cvt_pk_fp8_f32 v5, v8, v9
	v_cvt_pk_fp8_f32 v122, v126, v127 op_sel:[0,0,1]
	v_cvt_pk_fp8_f32 v124, v114, v115 op_sel:[0,0,1]
	s_addc_u32 s35, s89, s35
	v_pk_mul_f32 v[110:111], v[112:113], s[44:45] op_sel_hi:[1,0]
	v_cvt_pk_fp8_f32 v44, v46, v47 op_sel:[0,0,1]
	v_pk_mul_f32 v[32:33], v[56:57], s[44:45] op_sel_hi:[1,0]
	v_lshl_add_u64 v[114:115], s[34:35], 0, v[136:137]
	v_cvt_pk_fp8_f32 v106, v110, v111 op_sel:[0,0,1]
	v_pk_mul_f32 v[94:95], v[96:97], s[44:45] op_sel_hi:[1,0]
	s_movk_i32 s6, 0x1000
	v_cvt_pk_fp8_f32 v21, v32, v33 op_sel:[0,0,1]
	v_pk_mul_f32 v[16:17], v[40:41], s[44:45] op_sel_hi:[1,0]
	v_cvt_pk_fp8_f32 v91, v94, v95 op_sel:[0,0,1]
	v_pk_mul_f32 v[78:79], v[80:81], s[44:45] op_sel_hi:[1,0]
	v_pk_mul_f32 v[60:61], v[60:61], s[44:45] op_sel_hi:[1,0]
	v_add_co_u32_e32 v46, vcc, s6, v114
	v_cvt_pk_fp8_f32 v13, v16, v17 op_sel:[0,0,1]
	v_pk_mul_f32 v[6:7], v[24:25], s[44:45] op_sel_hi:[1,0]
	v_pk_mul_f32 v[8:9], v[28:29], s[44:45] op_sel_hi:[1,0]
	v_cvt_pk_fp8_f32 v75, v78, v79 op_sel:[0,0,1]
	v_cvt_pk_fp8_f32 v77, v60, v61 op_sel:[0,0,1]
	v_addc_co_u32_e32 v47, vcc, 0, v115, vcc
	v_cvt_pk_fp8_f32 v4, v6, v7 op_sel:[0,0,1]
	v_cvt_pk_fp8_f32 v5, v8, v9 op_sel:[0,0,1]
	global_store_dwordx4 v[114:115], v[122:125], off nt
	global_store_dwordx4 v[114:115], v[106:109], off offset:1024 nt
	global_store_dwordx4 v[114:115], v[90:93], off offset:2048 nt
	global_store_dwordx4 v[114:115], v[74:77], off offset:3072 nt
	global_store_dwordx4 v[46:47], v[42:45], off nt
	global_store_dwordx4 v[46:47], v[18:21], off offset:1024 nt
	global_store_dwordx4 v[46:47], v[10:13], off offset:2048 nt
	global_store_dwordx4 v[46:47], v[2:5], off offset:3072 nt
	s_and_b64 vcc, exec, s[0:1]
	s_mov_b64 s[0:1], -1
	s_cbranch_vccnz .LBB0_251
